# adds: x1 rows of the final phase touched at the end of the gate/up phase (prefetch to memory-side cache)
# speedup vs baseline: 1.0071x; 1.0071x over previous
; #define GAS __attribute__((address_space(1)))
; __device__ __forceinline__ int lane_id_v() { int l; asm volatile("v_mbcnt_lo_u32_b32 %0, -1, 0\n\tv_mbcnt_hi_u32_b32 %0, -1, %0" : "=v"(l)); return l; }
; #define BOTH(k) (IN(k) && IN((k) + 1))
; #define GRID_BAR() xcd_barrier(bar, TID())
; __global__ void __launch_bounds__(512, 2) hymba_fwd(Args args) {
;     ...
;                 if (ti >= 0) { const int lane = lane_id_v(); const int q = (CV_N5 + tailb * 8 - 1) / (tailb * 8), x0 = (ti * 8 + wave) * q, x1 = (x0 + q < CV_N5) ? x0 + q : CV_N5;
;                     convert_range(args.w_gate, args.w_up, args.w_down, BTGU, BTD, CV_GU + CV_D - CV_N5 + x0, CV_GU + CV_D - CV_N5 + x1, lds + wave * 8448, lane); }
;             }
;             if (BOTH(5)) GRID_BAR();
;     ...
;             auto ld = [&](int k) { const int t = tq + k * NGW; const int c0 = cc0[k], c1 = cc1[k];
;                 const size_t r0 = (size_t)(256 * tb[c0 >> 16] + (c0 & 0xffff)), r1 = (size_t)(256 * tb[c1 >> 16] + (c1 & 0xffff));
;                 const GAS v2u* xo = (const GAS v2u*)(X1B + (size_t)t * DM) + lane; const GAS unsigned* y0 = (const GAS unsigned*)((const unsigned char*)Yb + r0 * DM) + lane; const GAS unsigned* y1 = (const GAS unsigned*)((const unsigned char*)Yb + r1 * DM) + lane;
; #pragma unroll
;                 for (int j = 0; j < 8; ++j) { xb[k & 1][j] = __builtin_nontemporal_load(xo + 64 * j); b0[k & 1][j] = __builtin_nontemporal_load(y0 + 64 * j); b1[k & 1][j] = __builtin_nontemporal_load(y1 + 64 * j); } };
.LBB0_783:
	s_cmpk_lg_i32 s3, 0x100
	s_cbranch_scc1 .Lpf_skip
	s_lshl_b32 s100, s34, 12
	s_add_u32 s100, s26, s100
	s_addc_u32 s101, s27, 0
	s_add_u32 s100, s100, 0x5000000
	s_addc_u32 s101, s101, 0
	v_mbcnt_lo_u32_b32 v100, -1, 0
	v_mbcnt_hi_u32_b32 v100, -1, v100
	v_lshlrev_b32_e32 v100, 4, v100
	global_load_dwordx4 v[104:107], v100, s[100:101]
	global_load_dwordx4 v[104:107], v100, s[100:101] offset:1024
	global_load_dwordx4 v[104:107], v100, s[100:101] offset:2048
	global_load_dwordx4 v[104:107], v100, s[100:101] offset:3072
	s_add_u32 s100, s100, 0x800000
	s_addc_u32 s101, s101, 0
	global_load_dwordx4 v[104:107], v100, s[100:101]
	global_load_dwordx4 v[104:107], v100, s[100:101] offset:1024
	global_load_dwordx4 v[104:107], v100, s[100:101] offset:2048
	global_load_dwordx4 v[104:107], v100, s[100:101] offset:3072
	s_add_u32 s100, s100, 0x800000
	s_addc_u32 s101, s101, 0
	global_load_dwordx4 v[104:107], v100, s[100:101]
	global_load_dwordx4 v[104:107], v100, s[100:101] offset:1024
	global_load_dwordx4 v[104:107], v100, s[100:101] offset:2048
	global_load_dwordx4 v[104:107], v100, s[100:101] offset:3072
	s_add_u32 s100, s100, 0x800000
	s_addc_u32 s101, s101, 0
	global_load_dwordx4 v[104:107], v100, s[100:101]
	global_load_dwordx4 v[104:107], v100, s[100:101] offset:1024
	global_load_dwordx4 v[104:107], v100, s[100:101] offset:2048
	global_load_dwordx4 v[104:107], v100, s[100:101] offset:3072
